# energy workspace re-laid out per block (whole 128B lines written by one workgroup, no cross-XCD partial lines); softmax reads 32B per thread and writes coalesced; on top of v23
# baseline (speedup 1.0000x reference)
.LBB1_2:
	s_or_b64 exec, exec, s[0:1]
	s_lshr_b32 s8, s3, 6
	s_add_i32 s8, s8, s2
	s_and_b32 s8, s8, 15
	s_lshl_b32 s0, s2, 7
	v_and_b32_e32 v24, 63, v0
	s_add_i32 s9, s8, s0
	s_waitcnt lgkmcnt(0)
	s_and_b32 s1, s5, 0xffff
	s_mov_b32 s3, 0x20000
	s_brev_b32 s2, 16
	s_mov_b32 s0, s4
	v_lshlrev_b32_e32 v25, 4, v24
	s_lshl_b32 s4, s9, 12
	buffer_load_dwordx4 v[26:29], v25, s[0:3], s4 offen offset:1024 nt
	buffer_load_dwordx4 v[30:33], v25, s[0:3], s4 offen nt
	buffer_load_dwordx4 v[34:37], v25, s[0:3], s4 offen offset:2048 nt
	s_barrier
	s_add_i32 s5, s4, 0x10000
	buffer_load_dwordx4 v[38:41], v25, s[0:3], s5 offen offset:1024 nt
	buffer_load_dwordx4 v[42:45], v25, s[0:3], s5 offen nt
	buffer_load_dwordx4 v[16:19], v25, s[0:3], s4 offen offset:3072 nt
	s_add_i32 s10, s4, 0x20000
	buffer_load_dwordx4 v[46:49], v25, s[0:3], s5 offen offset:2048 nt
	buffer_load_dwordx4 v[20:23], v25, s[0:3], s5 offen offset:3072 nt
	buffer_load_dwordx4 v[50:53], v25, s[0:3], s10 offen offset:1024 nt
	buffer_load_dwordx4 v[54:57], v25, s[0:3], s10 offen nt
	ds_read_b128 v[4:7], v25 offset:1024
	ds_read_b128 v[0:3], v25
	ds_read_b128 v[12:15], v25 offset:2048
	ds_read_b128 v[8:11], v25 offset:3072
	s_add_i32 s5, s4, 0x30000
	v_cmp_gt_u32_e32 vcc, 8, v24
	s_waitcnt vmcnt(9) lgkmcnt(3)
	v_pk_mul_f32 v[28:29], v[6:7], v[28:29]
	v_pk_mul_f32 v[26:27], v[4:5], v[26:27]
	s_waitcnt vmcnt(8) lgkmcnt(2)
	v_pk_fma_f32 v[32:33], v[2:3], v[32:33], v[28:29]
	v_pk_fma_f32 v[30:31], v[0:1], v[30:31], v[26:27]
	buffer_load_dwordx4 v[26:29], v25, s[0:3], s5 offen offset:1024 nt
	s_waitcnt vmcnt(8) lgkmcnt(1)
	v_pk_fma_f32 v[58:59], v[14:15], v[36:37], v[32:33]
	v_pk_fma_f32 v[60:61], v[12:13], v[34:35], v[30:31]
	buffer_load_dwordx4 v[30:33], v25, s[0:3], s5 offen nt
	s_waitcnt vmcnt(8)
	v_pk_mul_f32 v[34:35], v[6:7], v[40:41]
	v_pk_mul_f32 v[36:37], v[4:5], v[38:39]
	s_waitcnt vmcnt(7)
	v_pk_fma_f32 v[44:45], v[2:3], v[44:45], v[34:35]
	v_pk_fma_f32 v[42:43], v[0:1], v[42:43], v[36:37]
	buffer_load_dwordx4 v[34:37], v25, s[0:3], s10 offen offset:2048 nt
	s_waitcnt vmcnt(4)
	v_pk_mul_f32 v[38:39], v[6:7], v[52:53]
	v_pk_mul_f32 v[40:41], v[4:5], v[50:51]
	s_waitcnt vmcnt(3)
	v_pk_fma_f32 v[50:51], v[2:3], v[56:57], v[38:39]
	v_pk_fma_f32 v[52:53], v[0:1], v[54:55], v[40:41]
	buffer_load_dwordx4 v[38:41], v25, s[0:3], s10 offen offset:3072 nt
	v_pk_fma_f32 v[48:49], v[14:15], v[48:49], v[44:45]
	v_pk_fma_f32 v[46:47], v[12:13], v[46:47], v[42:43]
	s_waitcnt lgkmcnt(0)
	v_pk_fma_f32 v[18:19], v[10:11], v[18:19], v[58:59]
	v_pk_fma_f32 v[16:17], v[8:9], v[16:17], v[60:61]
	v_add_f32_e32 v61, v18, v19
	v_add_f32_e32 v60, v16, v17
	v_pk_fma_f32 v[16:17], v[10:11], v[22:23], v[48:49]
	v_pk_fma_f32 v[18:19], v[8:9], v[20:21], v[46:47]
	v_add_f32_e32 v16, v16, v17
	v_add_f32_e32 v18, v18, v19
	v_add_f32_e32 v60, v60, v61
	v_add_f32_e32 v16, v18, v16
	s_add_i32 s10, s4, 0x50000
	s_waitcnt vmcnt(3)
	v_pk_mul_f32 v[28:29], v[6:7], v[28:29]
	v_pk_mul_f32 v[26:27], v[4:5], v[26:27]
	v_add_f32_dpp v16, v16, v16 quad_perm:[1,0,3,2] row_mask:0xf bank_mask:0xf bound_ctrl:1
	s_waitcnt vmcnt(2)
	v_pk_fma_f32 v[54:55], v[2:3], v[32:33], v[28:29]
	v_pk_fma_f32 v[56:57], v[0:1], v[30:31], v[26:27]
	buffer_load_dwordx4 v[26:29], v25, s[0:3], s5 offen offset:2048 nt
	buffer_load_dwordx4 v[30:33], v25, s[0:3], s5 offen offset:3072 nt
	s_add_i32 s5, s4, 0x40000
	buffer_load_dwordx4 v[42:45], v25, s[0:3], s5 offen offset:1024 nt
	s_waitcnt vmcnt(4)
	v_pk_fma_f32 v[50:51], v[14:15], v[36:37], v[50:51]
	v_pk_fma_f32 v[52:53], v[12:13], v[34:35], v[52:53]
	buffer_load_dwordx4 v[34:37], v25, s[0:3], s5 offen nt
	v_add_f32_dpp v16, v16, v16 quad_perm:[2,3,0,1] row_mask:0xf bank_mask:0xf bound_ctrl:1
	s_waitcnt vmcnt(4)
	v_pk_fma_f32 v[58:59], v[10:11], v[40:41], v[50:51]
	v_pk_fma_f32 v[38:39], v[8:9], v[38:39], v[52:53]
	v_add_f32_e32 v19, v58, v59
	v_add_f32_e32 v17, v38, v39
	v_add_f32_dpp v58, v60, v60 quad_perm:[1,0,3,2] row_mask:0xf bank_mask:0xf bound_ctrl:1
	v_add_f32_e32 v18, v17, v19
	v_add_f32_dpp v16, v16, v16 row_ror:4 row_mask:0xf bank_mask:0xf bound_ctrl:1
	v_add_f32_dpp v17, v58, v58 quad_perm:[2,3,0,1] row_mask:0xf bank_mask:0xf bound_ctrl:1
	buffer_load_dwordx4 v[20:23], v25, s[0:3], s5 offen offset:2048 nt
	buffer_load_dwordx4 v[46:49], v25, s[0:3], s5 offen offset:3072 nt
	v_add_f32_dpp v17, v17, v17 row_ror:4 row_mask:0xf bank_mask:0xf bound_ctrl:1
	v_add_f32_dpp v58, v16, v16 row_ror:8 row_mask:0xf bank_mask:0xf bound_ctrl:1
	buffer_load_dwordx4 v[38:41], v25, s[0:3], s10 offen nt
	buffer_load_dwordx4 v[50:53], v25, s[0:3], s10 offen offset:1024 nt
	v_add_f32_dpp v17, v17, v17 row_ror:8 row_mask:0xf bank_mask:0xf bound_ctrl:1
	v_mov_b32_e32 v19, v17
	v_mov_b32_e32 v59, v58
	s_nop 0
	v_permlane16_swap_b32_e32 v17, v19
	v_permlane16_swap_b32_e32 v58, v59
	v_add_f32_e32 v16, v17, v19
	v_add_f32_e32 v17, v58, v59
	s_add_i32 s5, s4, 0x60000
	s_add_i32 s4, s4, 0x70000
	v_add_f32_dpp v18, v18, v18 quad_perm:[1,0,3,2] row_mask:0xf bank_mask:0xf bound_ctrl:1
	s_waitcnt vmcnt(7)
	v_pk_fma_f32 v[28:29], v[14:15], v[28:29], v[54:55]
	v_pk_fma_f32 v[54:55], v[12:13], v[26:27], v[56:57]
	s_waitcnt vmcnt(6)
	v_pk_fma_f32 v[58:59], v[10:11], v[32:33], v[28:29]
	buffer_load_dwordx4 v[26:29], v25, s[0:3], s10 offen offset:2048 nt
	v_pk_fma_f32 v[54:55], v[8:9], v[30:31], v[54:55]
	buffer_load_dwordx4 v[30:33], v25, s[0:3], s10 offen offset:3072 nt
	v_add_f32_e32 v66, v54, v55
	s_waitcnt vmcnt(7)
	v_pk_mul_f32 v[54:55], v[6:7], v[44:45]
	v_pk_mul_f32 v[56:57], v[4:5], v[42:43]
	buffer_load_dwordx4 v[42:45], v25, s[0:3], s5 offen offset:1024 nt
	s_waitcnt vmcnt(7)
	v_pk_fma_f32 v[54:55], v[2:3], v[36:37], v[54:55]
	v_pk_fma_f32 v[56:57], v[0:1], v[34:35], v[56:57]
	buffer_load_dwordx4 v[34:37], v25, s[0:3], s5 offen nt
	v_add_f32_dpp v18, v18, v18 quad_perm:[2,3,0,1] row_mask:0xf bank_mask:0xf bound_ctrl:1
	s_waitcnt vmcnt(7)
	v_pk_fma_f32 v[22:23], v[14:15], v[22:23], v[54:55]
	v_pk_fma_f32 v[20:21], v[12:13], v[20:21], v[56:57]
	s_waitcnt vmcnt(6)
	v_pk_fma_f32 v[60:61], v[10:11], v[48:49], v[22:23]
	v_pk_fma_f32 v[22:23], v[8:9], v[46:47], v[20:21]
	s_waitcnt vmcnt(4)
	v_pk_mul_f32 v[54:55], v[4:5], v[50:51]
	v_pk_mul_f32 v[20:21], v[6:7], v[52:53]
	v_pk_fma_f32 v[38:39], v[0:1], v[38:39], v[54:55]
	buffer_load_dwordx4 v[46:49], v25, s[0:3], s5 offen offset:2048 nt
	buffer_load_dwordx4 v[50:53], v25, s[0:3], s5 offen offset:3072 nt
	v_pk_fma_f32 v[20:21], v[2:3], v[40:41], v[20:21]
	v_add_f32_e32 v23, v22, v23
	v_add_f32_dpp v18, v18, v18 row_ror:4 row_mask:0xf bank_mask:0xf bound_ctrl:1
	s_waitcnt vmcnt(5)
	v_pk_fma_f32 v[26:27], v[12:13], v[26:27], v[38:39]
	buffer_load_dwordx4 v[38:41], v25, s[0:3], s4 offen nt
	buffer_load_dwordx4 v[54:57], v25, s[0:3], s4 offen offset:1024 nt
	v_pk_fma_f32 v[20:21], v[14:15], v[28:29], v[20:21]
	s_waitcnt vmcnt(6)
	v_pk_fma_f32 v[30:31], v[8:9], v[30:31], v[26:27]
	v_pk_fma_f32 v[62:63], v[10:11], v[32:33], v[20:21]
	v_add_f32_dpp v18, v18, v18 row_ror:8 row_mask:0xf bank_mask:0xf bound_ctrl:1
	s_waitcnt vmcnt(5)
	v_pk_mul_f32 v[20:21], v[6:7], v[44:45]
	v_pk_mul_f32 v[26:27], v[4:5], v[42:43]
	buffer_load_dwordx4 v[42:45], v25, s[0:3], s4 offen offset:2048 nt
	s_waitcnt vmcnt(5)
	v_pk_fma_f32 v[64:65], v[0:1], v[34:35], v[26:27]
	buffer_load_dwordx4 v[32:35], v25, s[0:3], s4 offen offset:3072 nt
	v_add_f32_e32 v27, v60, v61
	v_add_f32_e32 v23, v23, v27
	v_pk_fma_f32 v[36:37], v[2:3], v[36:37], v[20:21]
	v_add_f32_e32 v20, v58, v59
	v_add_f32_dpp v23, v23, v23 quad_perm:[1,0,3,2] row_mask:0xf bank_mask:0xf bound_ctrl:1
	v_add_f32_e32 v20, v66, v20
	v_mov_b32_e32 v19, v18
	v_add_f32_dpp v23, v23, v23 quad_perm:[2,3,0,1] row_mask:0xf bank_mask:0xf bound_ctrl:1
	v_add_f32_dpp v20, v20, v20 quad_perm:[1,0,3,2] row_mask:0xf bank_mask:0xf bound_ctrl:1
	v_permlane16_swap_b32_e32 v18, v19
	v_add_f32_dpp v23, v23, v23 row_ror:4 row_mask:0xf bank_mask:0xf bound_ctrl:1
	v_add_f32_dpp v20, v20, v20 quad_perm:[2,3,0,1] row_mask:0xf bank_mask:0xf bound_ctrl:1
	v_add_f32_e32 v18, v18, v19
	v_add_f32_dpp v23, v23, v23 row_ror:8 row_mask:0xf bank_mask:0xf bound_ctrl:1
	v_mov_b32_e32 v27, v23
	s_nop 1
	v_permlane16_swap_b32_e32 v23, v27
	v_add_f32_e32 v28, v23, v27
	v_add_f32_e32 v23, v30, v31
	s_waitcnt vmcnt(5)
	v_pk_fma_f32 v[30:31], v[14:15], v[48:49], v[36:37]
	v_pk_fma_f32 v[36:37], v[12:13], v[46:47], v[64:65]
	s_waitcnt vmcnt(4)
	v_pk_fma_f32 v[30:31], v[10:11], v[52:53], v[30:31]
	v_pk_fma_f32 v[36:37], v[8:9], v[50:51], v[36:37]
	v_add_f32_e32 v27, v62, v63
	v_add_f32_e32 v36, v36, v37
	v_add_f32_e32 v30, v30, v31
	v_add_f32_e32 v23, v23, v27
	v_add_f32_e32 v30, v36, v30
	v_add_f32_dpp v20, v20, v20 row_ror:4 row_mask:0xf bank_mask:0xf bound_ctrl:1
	v_add_f32_dpp v23, v23, v23 quad_perm:[1,0,3,2] row_mask:0xf bank_mask:0xf bound_ctrl:1
	v_add_f32_dpp v30, v30, v30 quad_perm:[1,0,3,2] row_mask:0xf bank_mask:0xf bound_ctrl:1
	v_add_f32_dpp v20, v20, v20 row_ror:8 row_mask:0xf bank_mask:0xf bound_ctrl:1
	v_add_f32_dpp v23, v23, v23 quad_perm:[2,3,0,1] row_mask:0xf bank_mask:0xf bound_ctrl:1
	v_add_f32_dpp v30, v30, v30 quad_perm:[2,3,0,1] row_mask:0xf bank_mask:0xf bound_ctrl:1
	v_mov_b32_e32 v21, v20
	v_add_f32_dpp v23, v23, v23 row_ror:4 row_mask:0xf bank_mask:0xf bound_ctrl:1
	v_add_f32_dpp v30, v30, v30 row_ror:4 row_mask:0xf bank_mask:0xf bound_ctrl:1
	v_permlane16_swap_b32_e32 v20, v21
	v_add_f32_dpp v23, v23, v23 row_ror:8 row_mask:0xf bank_mask:0xf bound_ctrl:1
	v_add_f32_dpp v30, v30, v30 row_ror:8 row_mask:0xf bank_mask:0xf bound_ctrl:1
	v_mov_b32_e32 v27, v23
	v_mov_b32_e32 v31, v30
	s_nop 0
	v_permlane16_swap_b32_e32 v23, v27
	v_permlane16_swap_b32_e32 v30, v31
	v_add_f32_e32 v21, v20, v21
	v_add_f32_e32 v23, v23, v27
	v_add_f32_e32 v30, v30, v31
	v_mov_b32_e32 v19, v16
	v_mov_b32_e32 v20, v17
	v_mov_b32_e32 v22, v18
	v_mov_b32_e32 v26, v21
	v_mov_b32_e32 v29, v28
	v_mov_b32_e32 v27, v23
	v_mov_b32_e32 v31, v30
	v_permlane32_swap_b32_e32 v16, v19
	v_permlane32_swap_b32_e32 v17, v20
	v_permlane32_swap_b32_e32 v18, v22
	v_permlane32_swap_b32_e32 v21, v26
	v_permlane32_swap_b32_e32 v28, v29
	v_permlane32_swap_b32_e32 v23, v27
	s_waitcnt vmcnt(2)
	v_pk_mul_f32 v[6:7], v[6:7], v[56:57]
	v_pk_mul_f32 v[4:5], v[4:5], v[54:55]
	v_pk_fma_f32 v[2:3], v[2:3], v[40:41], v[6:7]
	v_pk_fma_f32 v[0:1], v[0:1], v[38:39], v[4:5]
	v_permlane32_swap_b32_e32 v30, v31
	s_waitcnt vmcnt(1)
	v_pk_fma_f32 v[2:3], v[14:15], v[44:45], v[2:3]
	v_pk_fma_f32 v[0:1], v[12:13], v[42:43], v[0:1]
	s_waitcnt vmcnt(0)
	v_pk_fma_f32 v[2:3], v[10:11], v[34:35], v[2:3]
	v_pk_fma_f32 v[0:1], v[8:9], v[32:33], v[0:1]
	s_nop 0
	v_add_f32_e32 v0, v0, v1
	v_add_f32_e32 v1, v2, v3
	v_add_f32_e32 v0, v0, v1
	s_nop 1
	v_add_f32_dpp v0, v0, v0 quad_perm:[1,0,3,2] row_mask:0xf bank_mask:0xf bound_ctrl:1
	s_nop 1
	v_add_f32_dpp v0, v0, v0 quad_perm:[2,3,0,1] row_mask:0xf bank_mask:0xf bound_ctrl:1
	s_nop 1
	v_add_f32_dpp v0, v0, v0 row_ror:4 row_mask:0xf bank_mask:0xf bound_ctrl:1
	s_nop 1
	v_add_f32_dpp v0, v0, v0 row_ror:8 row_mask:0xf bank_mask:0xf bound_ctrl:1
	v_mov_b32_e32 v1, v0
	s_nop 1
	v_permlane16_swap_b32_e32 v0, v1
	v_add_f32_e32 v0, v0, v1
	v_mov_b32_e32 v1, v0
	s_nop 1
	v_permlane32_swap_b32_e32 v0, v1
	s_and_saveexec_b64 s[0:1], vcc
	s_cbranch_execz .LBB1_4
	v_add_f32_e32 v6, v16, v19
	v_cmp_eq_u32_e32 vcc, 0, v24
	v_add_f32_e32 v5, v17, v20
	v_add_f32_e32 v4, v18, v22
	v_cndmask_b32_e32 v6, 0, v6, vcc
	v_cmp_eq_u32_e32 vcc, 1, v24
	v_add_f32_e32 v3, v21, v26
	v_add_f32_e32 v2, v28, v29
	v_cndmask_b32_e32 v5, v6, v5, vcc
	v_cmp_eq_u32_e32 vcc, 2, v24
	v_add_f32_e32 v0, v0, v1
	v_add_f32_e32 v1, v30, v31
	v_cndmask_b32_e32 v4, v5, v4, vcc
	v_cmp_eq_u32_e32 vcc, 3, v24
	s_lshr_b32 s0, s9, 7
	s_lshl_b32 s0, s0, 9
	s_lshl_b32 s1, s8, 5
	s_add_i32 s0, s0, s1
	v_cndmask_b32_e32 v3, v4, v3, vcc
	v_cmp_eq_u32_e32 vcc, 4, v24
	s_add_u32 s0, s6, s0
	s_addc_u32 s1, s7, 0
	v_cndmask_b32_e32 v2, v3, v2, vcc
	v_add_f32_e32 v3, v23, v27
	v_cmp_eq_u32_e32 vcc, 5, v24
	s_nop 1
	v_cndmask_b32_e32 v2, v2, v3, vcc
	v_cmp_eq_u32_e32 vcc, 6, v24
	s_nop 1
	v_cndmask_b32_e32 v1, v2, v1, vcc
	v_cmp_eq_u32_e32 vcc, 7, v24
	s_nop 1
	v_cndmask_b32_e32 v2, v1, v0, vcc
	v_mov_b32_e32 v0, v24
	v_ashrrev_i32_e32 v1, 31, v0
	v_lshl_add_u64 v[0:1], v[0:1], 2, s[0:1]
	v_add_co_u32_e32 v0, vcc, 0x6000, v0
	s_nop 1
	v_addc_co_u32_e32 v1, vcc, 0, v1, vcc
	global_store_dword v[0:1], v2, off offset:64

_Z14softmax_kernelPKfPf:
	s_load_dwordx4 s[4:7], s[0:1], 0x0
	s_ashr_i32 s3, s2, 31
	s_lshl_b64 s[0:1], s[2:3], 5
	v_and_b32_e32 v1, 63, v0
	v_lshl_add_u32 v2, v1, 4, s2
	s_waitcnt lgkmcnt(0)
	s_add_u32 s0, s4, s0
	s_addc_u32 s1, s5, s1
	s_add_u32 s8, s4, 0x4000
	s_addc_u32 s9, s5, 0
	v_ashrrev_i32_e32 v3, 31, v2
	v_lshl_add_u64 v[4:5], v[2:3], 2, s[8:9]
	v_add_u32_e32 v2, 0x400, v2
	v_ashrrev_i32_e32 v3, 31, v2
	v_lshl_add_u64 v[2:3], v[2:3], 2, s[8:9]
	global_load_dword v14, v[4:5], off
	global_load_dword v15, v[2:3], off
	v_mov_b32_e32 v3, 0
	v_lshlrev_b32_e32 v2, 9, v0
	v_lshl_add_u64 v[8:9], s[0:1], 0, v[2:3]
	s_movk_i32 s0, 0x6000
	v_add_co_u32_e32 v4, vcc, s0, v8
	s_movk_i32 s0, 0x6010
	s_nop 0
	v_addc_co_u32_e32 v5, vcc, 0, v9, vcc
	v_add_co_u32_e32 v8, vcc, s0, v8
	global_load_dwordx4 v[4:7], v[4:5], off offset:64
	s_load_dword s1, s[4:5], 0x6000
	v_addc_co_u32_e32 v9, vcc, 0, v9, vcc
	global_load_dwordx4 v[10:13], v[8:9], off offset:64
	v_lshrrev_b32_e32 v16, 6, v0
	v_cmp_eq_u32_e32 vcc, 0, v1
	s_mov_b32 s0, 0xff800000
	s_waitcnt vmcnt(2)
	v_add_f32_e32 v0, v14, v15
	s_nop 1
	v_add_f32_dpp v0, v0, v0 quad_perm:[1,0,3,2] row_mask:0xf bank_mask:0xf bound_ctrl:1
	s_nop 1
	v_add_f32_dpp v0, v0, v0 quad_perm:[2,3,0,1] row_mask:0xf bank_mask:0xf bound_ctrl:1
	s_nop 1
	v_add_f32_dpp v0, v0, v0 row_ror:4 row_mask:0xf bank_mask:0xf bound_ctrl:1
	s_nop 1
	v_add_f32_dpp v0, v0, v0 row_ror:8 row_mask:0xf bank_mask:0xf bound_ctrl:1
	v_mov_b32_e32 v1, v0
	s_nop 1
	v_permlane16_swap_b32_e32 v0, v1
	v_add_f32_e32 v0, v0, v1
	v_mov_b32_e32 v1, v0
	s_nop 1
	v_permlane32_swap_b32_e32 v0, v1
	v_add_f32_e32 v0, v0, v1
	s_waitcnt lgkmcnt(0)
	v_add_f32_e32 v14, s1, v0
	s_waitcnt vmcnt(1)
	v_pk_add_f32 v[6:7], v[14:15], v[6:7] op_sel_hi:[0,1]
	s_waitcnt vmcnt(0)
	v_pk_add_f32 v[8:9], v[14:15], v[12:13] op_sel_hi:[0,1]
	v_pk_add_f32 v[0:1], v[14:15], v[4:5] op_sel_hi:[0,1]
	v_pk_add_f32 v[4:5], v[14:15], v[10:11] op_sel_hi:[0,1]
	v_max_f32_e32 v10, v6, v7
	v_max_f32_e32 v11, v8, v9
	v_max3_f32 v10, v0, v1, v10
	v_max3_f32 v11, v4, v5, v11
	v_max3_f32 v10, v10, s0, v11
	s_nop 1
	v_mov_b32_dpp v11, v10 quad_perm:[1,0,3,2] row_mask:0xf bank_mask:0xf bound_ctrl:1
	v_max_f32_e32 v11, v11, v11
	v_max_f32_e32 v10, v10, v11
	s_nop 1
	v_mov_b32_dpp v11, v10 quad_perm:[2,3,0,1] row_mask:0xf bank_mask:0xf bound_ctrl:1
	v_max_f32_e32 v11, v11, v11
	v_max_f32_e32 v10, v10, v11
	s_nop 1
	v_mov_b32_dpp v11, v10 row_ror:4 row_mask:0xf bank_mask:0xf bound_ctrl:1
	v_max_f32_e32 v11, v11, v11
	v_max_f32_e32 v10, v10, v11
	s_nop 1
	v_mov_b32_dpp v11, v10 row_ror:8 row_mask:0xf bank_mask:0xf bound_ctrl:1
	v_max_f32_e32 v11, v11, v11
	v_max_f32_e32 v10, v10, v11
	v_mov_b32_e32 v11, v10
	s_nop 1
	v_permlane16_swap_b32_e32 v10, v11
	v_max_f32_e32 v11, v11, v11
	v_max_f32_e32 v10, v10, v10
	v_max_f32_e32 v11, v10, v11
	v_mov_b32_e32 v12, v11
	s_nop 1
	v_permlane32_swap_b32_e32 v11, v12
	v_lshlrev_b32_e32 v10, 2, v16
	s_and_saveexec_b64 s[0:1], vcc
	v_max_f32_e32 v11, v11, v11
	v_max_f32_e32 v12, v12, v12
	v_max_f32_e32 v11, v11, v12
	ds_write_b32 v10, v11
	s_or_b64 exec, exec, s[0:1]
	s_waitcnt lgkmcnt(0)
	s_barrier
	ds_read_b128 v[12:15], v3
	s_lshl_b64 s[0:1], s[2:3], 11
	s_waitcnt lgkmcnt(0)
	v_max_f32_e32 v3, v15, v15
	v_max_f32_e32 v11, v14, v14
	v_max_f32_e32 v3, v11, v3
	v_max3_f32 v3, v12, v13, v3
	v_sub_f32_e32 v0, v0, v3
	v_mul_f32_e32 v0, 0x3fb8aa3b, v0
	v_sub_f32_e32 v1, v1, v3
	v_exp_f32_e32 v0, v0
	v_mul_f32_e32 v1, 0x3fb8aa3b, v1
	v_sub_f32_e32 v6, v6, v3
	v_exp_f32_e32 v1, v1
	v_mul_f32_e32 v6, 0x3fb8aa3b, v6
	v_sub_f32_e32 v7, v7, v3
	v_exp_f32_e32 v6, v6
	v_mul_f32_e32 v7, 0x3fb8aa3b, v7
	v_sub_f32_e32 v4, v4, v3
	v_exp_f32_e32 v7, v7
	v_mul_f32_e32 v4, 0x3fb8aa3b, v4
	v_sub_f32_e32 v5, v5, v3
	v_add_f32_e32 v11, 0, v0
	v_exp_f32_e32 v4, v4
	v_mul_f32_e32 v5, 0x3fb8aa3b, v5
	v_sub_f32_e32 v8, v8, v3
	v_add_f32_e32 v11, v11, v1
	v_exp_f32_e32 v5, v5
	v_mul_f32_e32 v8, 0x3fb8aa3b, v8
	v_sub_f32_e32 v3, v9, v3
	v_add_f32_e32 v11, v11, v6
	v_exp_f32_e32 v8, v8
	v_mul_f32_e32 v3, 0x3fb8aa3b, v3
	v_add_f32_e32 v11, v11, v7
	v_exp_f32_e32 v9, v3
	v_add_f32_e32 v3, v11, v4
	v_add_f32_e32 v3, v3, v5
	v_add_f32_e32 v3, v3, v8
	v_add_f32_e32 v3, v3, v9
	s_nop 1
	v_add_f32_dpp v3, v3, v3 quad_perm:[1,0,3,2] row_mask:0xf bank_mask:0xf bound_ctrl:1
	s_nop 1
	v_add_f32_dpp v3, v3, v3 quad_perm:[2,3,0,1] row_mask:0xf bank_mask:0xf bound_ctrl:1
	s_nop 1
	v_add_f32_dpp v3, v3, v3 row_ror:4 row_mask:0xf bank_mask:0xf bound_ctrl:1
	s_nop 1
	v_add_f32_dpp v3, v3, v3 row_ror:8 row_mask:0xf bank_mask:0xf bound_ctrl:1
	v_mov_b32_e32 v11, v3
	s_nop 1
	v_permlane16_swap_b32_e32 v3, v11
	v_add_f32_e32 v3, v3, v11
	v_mov_b32_e32 v11, v3
	s_nop 1
	v_permlane32_swap_b32_e32 v3, v11
	s_and_saveexec_b64 s[2:3], vcc
	v_add_f32_e32 v3, v3, v11
	ds_write_b32 v10, v3 offset:16
	s_or_b64 exec, exec, s[2:3]
	v_mov_b32_e32 v3, 0
	s_waitcnt lgkmcnt(0)
	s_barrier
	ds_read_b64 v[10:11], v3 offset:16
	ds_read2_b32 v[12:13], v3 offset0:5 offset1:6
	s_waitcnt lgkmcnt(1)
	ds_read_b32 v11, v3 offset:28
	s_lshl_b64 s[0:1], s[0:1], 2
	s_add_u32 s0, s6, s0
	s_addc_u32 s1, s7, s1
	s_waitcnt lgkmcnt(0)
	v_pk_add_f32 v[10:11], v[12:13], v[10:11]
	s_nop 0
	v_add_f32_e32 v10, v10, v11
	v_div_scale_f32 v11, s[2:3], v10, v10, 1.0
	v_rcp_f32_e32 v12, v11
	v_div_scale_f32 v13, vcc, 1.0, v10, 1.0
	v_fma_f32 v14, -v11, v12, 1.0
	v_fmac_f32_e32 v12, v14, v12
	v_mul_f32_e32 v14, v13, v12
	v_fma_f32 v15, -v11, v14, v13
	v_fmac_f32_e32 v14, v15, v12
	v_fma_f32 v11, -v11, v14, v13
	v_div_fmas_f32 v11, v11, v12, v14
	v_div_fixup_f32 v14, v11, v10, 1.0
	v_pk_mul_f32 v[12:13], v[14:15], v[6:7] op_sel_hi:[0,1]
	v_lshrrev_b32_e32 v2, 4, v2
	v_lshl_add_u64 v[6:7], s[0:1], 0, v[2:3]
	v_pk_mul_f32 v[10:11], v[14:15], v[0:1] op_sel_hi:[0,1]
	v_pk_mul_f32 v[0:1], v[14:15], v[4:5] op_sel_hi:[0,1]
	v_add_co_u32_e32 v4, vcc, 16, v6
	global_store_dwordx4 v2, v[10:13], s[0:1]
	v_pk_mul_f32 v[2:3], v[14:15], v[8:9] op_sel_hi:[0,1]
	v_addc_co_u32_e32 v5, vcc, 0, v7, vcc
	global_store_dwordx4 v[4:5], v[0:3], off
	s_endpgm
